# c39: c38 with the look-ahead loads skipped on a wave's last pass (no extra traffic, no wait at exit)
# speedup vs baseline: 1.0061x; 1.0061x over previous
; #define GAS __attribute__((address_space(1)))
; __global__ void __launch_bounds__(NTHREADS, 2) fwd(Args args) {
;     ...
;         for (int t0 = 2 * gw; t0 < SEQ; t0 += 2 * NGW) {
;             unsigned long long hr[2][4]; unsigned pr[2][2][4]; int sl[2][2];
; #pragma unroll
;             for (int r = 0; r < 2; ++r) { const int t = t0 + r;
;                 const GAS unsigned long long* hp = (const GAS unsigned long long*)(HN + (size_t)t * DM) + F.lane;
; #pragma unroll
;                 for (int q = 0; q < 4; ++q) hr[r][q] = __builtin_nontemporal_load(hp + 64 * q);
; #pragma unroll
;                 for (int k = 0; k < 2; ++k) { const GAS unsigned* pa = (const GAS unsigned*)((const unsigned char*)PAIR + (size_t)(2 * t + k) * DM) + F.lane;
; #pragma unroll
;                     for (int q = 0; q < 4; ++q) pr[r][k][q] = __builtin_nontemporal_load(pa + 64 * q);
;                     sl[r][k] = SLOTOF[2 * t + k]; } }
.Lfin_copy:
	v_mov_b32_e32 v16, v192
	v_mov_b32_e32 v17, v193
	v_mov_b32_e32 v18, v194
	v_mov_b32_e32 v19, v195
	v_mov_b32_e32 v20, v196
	v_mov_b32_e32 v21, v197
	v_mov_b32_e32 v22, v198
	v_mov_b32_e32 v23, v199
	v_mov_b32_e32 v66, v200
	v_mov_b32_e32 v67, v201
	v_mov_b32_e32 v64, v202
	v_mov_b32_e32 v65, v203
	v_mov_b32_e32 v62, v204
	v_mov_b32_e32 v63, v205
	v_mov_b32_e32 v60, v206
	v_mov_b32_e32 v61, v207
	v_mov_b32_e32 v188, v208
	v_mov_b32_e32 v189, v209
	v_mov_b32_e32 v190, v210
	v_mov_b32_e32 v191, v211
	v_mov_b32_e32 v95, v212
	v_mov_b32_e32 v94, v213
	v_mov_b32_e32 v93, v214
	v_mov_b32_e32 v92, v215
	v_mov_b32_e32 v91, v216
	v_mov_b32_e32 v90, v217
	v_mov_b32_e32 v89, v218
	v_mov_b32_e32 v88, v219
	v_mov_b32_e32 v87, v220
	v_mov_b32_e32 v86, v221
	v_mov_b32_e32 v85, v222
	v_mov_b32_e32 v84, v223
	v_mov_b32_e32 v26, v224
	v_mov_b32_e32 v27, v225
	v_mov_b32_e32 v28, v226
	v_mov_b32_e32 v29, v227
	s_cmpk_lt_i32 s25, 0x2000
	s_cbranch_scc0 .Lfin_skipnp
	s_add_i32 s44, s4, 0x2000
	s_ashr_i32 s45, s44, 31
	s_lshl_b64 s[46:47], s[44:45], 10
	s_lshl_b64 s[44:45], s[44:45], 2
	s_add_u32 s44, s7, s44
	s_addc_u32 s45, s20, s45
	v_lshl_add_u64 v[228:229], v[54:55], 0, s[46:47]
	v_lshl_add_u64 v[230:231], v[58:59], 0, s[10:11]
	global_load_dwordx2 v[192:193], v[230:231], off nt
	global_load_dwordx2 v[194:195], v[230:231], off offset:512 nt
	global_load_dwordx2 v[196:197], v[230:231], off offset:1024 nt
	global_load_dwordx2 v[198:199], v[230:231], off offset:1536 nt
	global_load_dwordx2 v[200:201], v[230:231], off offset:2048 nt
	global_load_dwordx2 v[202:203], v[230:231], off offset:2560 nt
	global_load_dwordx2 v[204:205], v[230:231], off offset:3072 nt
	global_load_dwordx2 v[206:207], v[230:231], off offset:3584 nt
	global_load_dword v208, v[228:229], off nt
	global_load_dword v209, v[228:229], off offset:256 nt
	global_load_dword v210, v[228:229], off offset:512 nt
	global_load_dword v211, v[228:229], off offset:768 nt
	global_load_dword v212, v[228:229], off offset:1024 nt
	global_load_dword v213, v[228:229], off offset:1280 nt
	global_load_dword v214, v[228:229], off offset:1536 nt
	global_load_dword v215, v[228:229], off offset:1792 nt
	global_load_dword v216, v[228:229], off offset:2048 nt
	global_load_dword v217, v[228:229], off offset:2304 nt
	global_load_dword v218, v[228:229], off offset:2560 nt
	global_load_dword v219, v[228:229], off offset:2816 nt
	global_load_dword v220, v[228:229], off offset:3072 nt
	global_load_dword v221, v[228:229], off offset:3328 nt
	global_load_dword v222, v[228:229], off offset:3584 nt
	global_load_dword v223, v[228:229], off offset:3840 nt
	global_load_dword v224, v53, s[44:45]
	global_load_dword v225, v53, s[44:45] offset:4
	global_load_dword v226, v53, s[44:45] offset:8
	global_load_dword v227, v53, s[44:45] offset:12
.Lfin_skipnp:
	s_ashr_i32 s5, s4, 31
	s_lshl_b64 s[42:43], s[4:5], 10
	s_lshl_b64 s[16:17], s[4:5], 2
	s_add_u32 s18, s7, s16
	s_addc_u32 s19, s20, s17
	s_add_i32 s0, s4, 1
	s_ashr_i32 s1, s0, 31
	s_lshl_b64 s[12:13], s[0:1], 10
	s_lshl_b64 s[0:1], s[0:1], 2
	s_add_u32 s34, s7, s0
	s_addc_u32 s35, s20, s1
	s_add_i32 s12, s4, 2
	s_ashr_i32 s13, s12, 31
	s_lshl_b64 s[14:15], s[12:13], 10
	s_lshl_b64 s[14:15], s[12:13], 2
	s_add_u32 s36, s7, s14
	s_addc_u32 s37, s20, s15
	s_add_i32 s12, s4, 3
	s_ashr_i32 s13, s12, 31
	s_lshl_b64 s[38:39], s[12:13], 10
	s_lshl_b64 s[12:13], s[12:13], 2
	s_add_u32 s38, s7, s12
	s_addc_u32 s39, s20, s13
	s_mov_b64 s[18:19], -1
	v_lshlrev_b32_e32 v52, 4, v162
	v_lshlrev_b32_e32 v44, 16, v16
	v_and_b32_e32 v45, 0xffff0000, v16
	v_alignbit_b32 v16, v17, v16, 16
	v_and_b32_e32 v47, 0xffff0000, v17
	v_lshlrev_b32_e32 v48, 16, v18
	v_and_b32_e32 v49, 0xffff0000, v18
	v_alignbit_b32 v17, v19, v18, 16
	v_and_b32_e32 v51, 0xffff0000, v19
	v_alignbit_b32 v18, v21, v20, 16
	v_alignbit_b32 v19, v23, v22, 16
	v_readfirstlane_b32 s37, v26
	s_ashr_i32 s2, s37, 8
	v_lshlrev_b32_e32 v70, 16, v20
	v_and_b32_e32 v71, 0xffff0000, v20
	v_and_b32_e32 v73, 0xffff0000, v21
	v_lshlrev_b32_e32 v68, 16, v22
	v_and_b32_e32 v69, 0xffff0000, v22
	v_and_b32_e32 v75, 0xffff0000, v23
	v_and_b32_e32 v46, 0xffff0000, v16
	v_and_b32_e32 v50, 0xffff0000, v17
	v_and_b32_e32 v72, 0xffff0000, v18
	v_and_b32_e32 v74, 0xffff0000, v19
	s_cmpk_gt_i32 s2, 0x7f
	v_readfirstlane_b32 s36, v27
	v_readfirstlane_b32 s35, v28
	v_readfirstlane_b32 s34, v29
	s_cbranch_scc0 .LBB0_1481
; #define GAS __attribute__((address_space(1)))
; __global__ void __launch_bounds__(NTHREADS, 2) fwd(Args args) {
;     ...
;                     } else { const int lt = (slot >> 8) - 128, rl = slot & 255; const float gt = GATES[2 * t + k] * (1.0f / 32.0f);
; #pragma unroll
;                         for (int q = 0; q < 4; ++q) { const GAS f32x4* pp = (const GAS f32x4*)(PART + (size_t)((lt * 4 + q) * 7) * 65536 + rl * 256) + F.lane; f32x4 s = pp[0];
; #pragma unroll
;                             for (int s7 = 1; s7 < 7; ++s7) s += pp[(size_t)s7 * 16384];
	s_add_u32 s38, s21, s16
	s_addc_u32 s39, s22, s17
	s_lshl_b32 s16, s37, 10
	s_and_b32 s16, s16, 0x3fc00
	s_add_u32 s16, s23, s16
	s_mul_i32 s18, s2, 28
	s_addc_u32 s17, s24, 0
	s_add_i32 s2, s18, 0xfffff200
	s_lshl_b64 s[40:41], s[2:3], 18
	s_add_u32 s40, s16, s40
	s_addc_u32 s41, s17, s41
	v_lshl_add_u64 v[36:37], s[40:41], 0, v[52:53]
	v_add_co_u32_e32 v28, vcc, s26, v36
	s_add_i32 s2, s18, 0xfffff207
	s_nop 0
	v_addc_co_u32_e32 v29, vcc, 0, v37, vcc
	v_add_co_u32_e32 v30, vcc, s27, v36
	global_load_dword v163, v53, s[38:39]
	global_load_dwordx4 v[16:19], v52, s[40:41]
	v_addc_co_u32_e32 v31, vcc, 0, v37, vcc
	v_add_co_u32_e32 v38, vcc, s28, v36
	s_lshl_b64 s[38:39], s[2:3], 18
	s_nop 0
	v_addc_co_u32_e32 v39, vcc, 0, v37, vcc
	v_add_co_u32_e32 v40, vcc, s29, v36
	s_add_u32 s38, s16, s38
	s_nop 0
	v_addc_co_u32_e32 v41, vcc, 0, v37, vcc
	v_add_co_u32_e32 v96, vcc, s30, v36
	s_addc_u32 s39, s17, s39
	s_nop 0
	v_addc_co_u32_e32 v97, vcc, 0, v37, vcc
	v_add_co_u32_e32 v98, vcc, s31, v36
	v_lshl_add_u64 v[112:113], s[38:39], 0, v[52:53]
	s_nop 0
	v_addc_co_u32_e32 v99, vcc, 0, v37, vcc
	v_add_co_u32_e32 v104, vcc, s26, v112
	s_add_i32 s2, s18, 0xfffff20e
	s_nop 0
	v_addc_co_u32_e32 v105, vcc, 0, v113, vcc
	v_add_co_u32_e32 v106, vcc, s27, v112
	s_lshl_b64 s[40:41], s[2:3], 18
	s_nop 0
	v_addc_co_u32_e32 v107, vcc, 0, v113, vcc
	v_add_co_u32_e32 v114, vcc, s28, v112
	s_add_u32 s40, s16, s40
	s_nop 0
	v_addc_co_u32_e32 v115, vcc, 0, v113, vcc
	v_add_co_u32_e32 v116, vcc, s29, v112
	s_addc_u32 s41, s17, s41
	s_nop 0
	v_addc_co_u32_e32 v117, vcc, 0, v113, vcc
	v_add_co_u32_e32 v120, vcc, s30, v112
	v_lshl_add_u64 v[144:145], s[40:41], 0, v[52:53]
	s_nop 0
	v_addc_co_u32_e32 v121, vcc, 0, v113, vcc
	v_add_co_u32_e32 v122, vcc, s31, v112
	s_add_i32 s2, s18, 0xfffff215
	s_nop 0
	v_addc_co_u32_e32 v123, vcc, 0, v113, vcc
	v_add_co_u32_e32 v128, vcc, s26, v144
	global_load_dwordx4 v[20:23], v[28:29], off
	global_load_dwordx4 v[24:27], v[30:31], off
	v_addc_co_u32_e32 v129, vcc, 0, v145, vcc
	v_add_co_u32_e32 v132, vcc, s27, v144
	global_load_dwordx4 v[28:31], v[38:39], off
	global_load_dwordx4 v[32:35], v[40:41], off
	v_addc_co_u32_e32 v133, vcc, 0, v145, vcc
	v_add_co_u32_e32 v136, vcc, s28, v144
	global_load_dwordx4 v[36:39], v[96:97], off
	global_load_dwordx4 v[40:43], v[98:99], off
	v_addc_co_u32_e32 v137, vcc, 0, v145, vcc
	v_add_co_u32_e32 v140, vcc, s29, v144
	global_load_dwordx4 v[96:99], v[104:105], off
	global_load_dwordx4 v[100:103], v[106:107], off
	v_addc_co_u32_e32 v141, vcc, 0, v145, vcc
	global_load_dwordx4 v[104:107], v[114:115], off
	global_load_dwordx4 v[108:111], v[116:117], off
	s_nop 0
	global_load_dwordx4 v[112:115], v[120:121], off
	global_load_dwordx4 v[116:119], v[122:123], off
	s_nop 0
	global_load_dwordx4 v[120:123], v52, s[38:39]
	global_load_dwordx4 v[124:127], v52, s[40:41]
	v_add_co_u32_e32 v146, vcc, s30, v144
	s_lshl_b64 s[18:19], s[2:3], 18
	s_waitcnt lgkmcnt(0)
	v_addc_co_u32_e32 v147, vcc, 0, v145, vcc
	s_add_u32 s16, s16, s18
	v_add_co_u32_e32 v148, vcc, s31, v144
	s_addc_u32 s17, s17, s19
	s_nop 0
	v_addc_co_u32_e32 v149, vcc, 0, v145, vcc
	v_lshl_add_u64 v[160:161], s[16:17], 0, v[52:53]
	v_add_co_u32_e32 v156, vcc, s26, v160
	global_load_dwordx4 v[128:131], v[128:129], off
	s_nop 0
	global_load_dwordx4 v[132:135], v[132:133], off
	v_addc_co_u32_e32 v157, vcc, 0, v161, vcc
	v_add_co_u32_e32 v164, vcc, s27, v160
	global_load_dwordx4 v[136:139], v[136:137], off
	s_nop 0
	global_load_dwordx4 v[140:143], v[140:141], off
	v_addc_co_u32_e32 v165, vcc, 0, v161, vcc
	v_add_co_u32_e32 v168, vcc, s28, v160
	global_load_dwordx4 v[144:147], v[146:147], off
	s_nop 0
	global_load_dwordx4 v[148:151], v[148:149], off
	v_addc_co_u32_e32 v169, vcc, 0, v161, vcc
	v_add_co_u32_e32 v172, vcc, s29, v160
	global_load_dwordx4 v[152:155], v52, s[16:17]
	s_nop 0
	v_addc_co_u32_e32 v173, vcc, 0, v161, vcc
	global_load_dwordx4 v[156:159], v[156:157], off
	s_nop 0
	global_load_dwordx4 v[164:167], v[164:165], off
	v_add_co_u32_e32 v176, vcc, s30, v160
	global_load_dwordx4 v[168:171], v[168:169], off
	s_nop 0
	global_load_dwordx4 v[172:175], v[172:173], off
	v_addc_co_u32_e32 v177, vcc, 0, v161, vcc
	v_add_co_u32_e32 v160, vcc, 0x180000, v160
	global_load_dwordx4 v[176:179], v[176:177], off
	s_nop 0
	v_addc_co_u32_e32 v161, vcc, 0, v161, vcc
	global_load_dwordx4 v[180:183], v[160:161], off
	s_waitcnt vmcnt(28)
; #define GAS __attribute__((address_space(1)))
; __global__ void __launch_bounds__(NTHREADS, 2) fwd(Args args) {
;     ...
;                     } else { const int lt = (slot >> 8) - 128, rl = slot & 255; const float gt = GATES[2 * t + k] * (1.0f / 32.0f);
; #pragma unroll
;                         for (int q = 0; q < 4; ++q) { const GAS f32x4* pp = (const GAS f32x4*)(PART + (size_t)((lt * 4 + q) * 7) * 65536 + rl * 256) + F.lane; f32x4 s = pp[0];
; #pragma unroll
;                             for (int s7 = 1; s7 < 7; ++s7) s += pp[(size_t)s7 * 16384];
;                             v[q] += s * gt; } } }
	v_mul_f32_e32 v160, 0x3d000000, v163
	s_waitcnt vmcnt(26)
	v_pk_add_f32 v[18:19], v[18:19], v[22:23]
	v_pk_add_f32 v[16:17], v[16:17], v[20:21]
	s_waitcnt vmcnt(25)
	v_pk_add_f32 v[18:19], v[18:19], v[26:27]
	v_pk_add_f32 v[16:17], v[16:17], v[24:25]
	s_waitcnt vmcnt(24)
	v_pk_add_f32 v[18:19], v[18:19], v[30:31]
	v_pk_add_f32 v[16:17], v[16:17], v[28:29]
	s_waitcnt vmcnt(23)
	v_pk_add_f32 v[18:19], v[18:19], v[34:35]
	v_pk_add_f32 v[16:17], v[16:17], v[32:33]
	s_waitcnt vmcnt(22)
	v_pk_add_f32 v[18:19], v[18:19], v[38:39]
	v_pk_add_f32 v[16:17], v[16:17], v[36:37]
	s_waitcnt vmcnt(21)
	v_pk_add_f32 v[18:19], v[18:19], v[42:43]
	v_pk_add_f32 v[16:17], v[16:17], v[40:41]
	v_pk_fma_f32 v[18:19], v[160:161], v[18:19], v[46:47] op_sel_hi:[0,1,1]
	v_pk_fma_f32 v[16:17], v[160:161], v[16:17], v[44:45] op_sel_hi:[0,1,1]
	s_waitcnt vmcnt(14)
	v_pk_add_f32 v[20:21], v[122:123], v[98:99]
	v_pk_add_f32 v[22:23], v[120:121], v[96:97]
	v_pk_add_f32 v[20:21], v[20:21], v[102:103]
	v_pk_add_f32 v[22:23], v[22:23], v[100:101]
	v_pk_add_f32 v[20:21], v[20:21], v[106:107]
	v_pk_add_f32 v[22:23], v[22:23], v[104:105]
	v_pk_add_f32 v[20:21], v[20:21], v[110:111]
	v_pk_add_f32 v[22:23], v[22:23], v[108:109]
	v_pk_add_f32 v[20:21], v[20:21], v[114:115]
	v_pk_add_f32 v[22:23], v[22:23], v[112:113]
	v_pk_add_f32 v[20:21], v[20:21], v[118:119]
	v_pk_add_f32 v[24:25], v[22:23], v[116:117]
	v_pk_fma_f32 v[22:23], v[160:161], v[20:21], v[50:51] op_sel_hi:[0,1,1]
	v_pk_fma_f32 v[20:21], v[160:161], v[24:25], v[48:49] op_sel_hi:[0,1,1]
	s_waitcnt vmcnt(12)
	v_pk_add_f32 v[24:25], v[126:127], v[130:131]
	v_pk_add_f32 v[26:27], v[124:125], v[128:129]
	s_waitcnt vmcnt(11)
	v_pk_add_f32 v[24:25], v[24:25], v[134:135]
	v_pk_add_f32 v[26:27], v[26:27], v[132:133]
	s_waitcnt vmcnt(10)
	v_pk_add_f32 v[24:25], v[24:25], v[138:139]
	v_pk_add_f32 v[26:27], v[26:27], v[136:137]
	s_waitcnt vmcnt(9)
	v_pk_add_f32 v[24:25], v[24:25], v[142:143]
	v_pk_add_f32 v[26:27], v[26:27], v[140:141]
	s_waitcnt vmcnt(8)
	v_pk_add_f32 v[24:25], v[24:25], v[146:147]
	v_pk_add_f32 v[26:27], v[26:27], v[144:145]
	s_waitcnt vmcnt(7)
	v_pk_add_f32 v[24:25], v[24:25], v[150:151]
	v_pk_add_f32 v[28:29], v[26:27], v[148:149]
	v_pk_fma_f32 v[26:27], v[160:161], v[24:25], v[72:73] op_sel_hi:[0,1,1]
	v_pk_fma_f32 v[24:25], v[160:161], v[28:29], v[70:71] op_sel_hi:[0,1,1]
	s_waitcnt vmcnt(5)
	v_pk_add_f32 v[28:29], v[154:155], v[158:159]
	v_pk_add_f32 v[30:31], v[152:153], v[156:157]
	s_waitcnt vmcnt(4)
	v_pk_add_f32 v[28:29], v[28:29], v[166:167]
	v_pk_add_f32 v[30:31], v[30:31], v[164:165]
	s_waitcnt vmcnt(3)
	v_pk_add_f32 v[28:29], v[28:29], v[170:171]
	v_pk_add_f32 v[30:31], v[30:31], v[168:169]
	s_waitcnt vmcnt(2)
	v_pk_add_f32 v[28:29], v[28:29], v[174:175]
	v_pk_add_f32 v[30:31], v[30:31], v[172:173]
	s_waitcnt vmcnt(1)
	v_pk_add_f32 v[28:29], v[28:29], v[178:179]
	v_pk_add_f32 v[30:31], v[30:31], v[176:177]
	s_waitcnt vmcnt(0)
	v_pk_add_f32 v[28:29], v[28:29], v[182:183]
	v_pk_add_f32 v[32:33], v[30:31], v[180:181]
	v_pk_fma_f32 v[30:31], v[160:161], v[28:29], v[74:75] op_sel_hi:[0,1,1]
	v_pk_fma_f32 v[28:29], v[160:161], v[32:33], v[68:69] op_sel_hi:[0,1,1]
	s_cbranch_execnz .LBB0_1483
	s_branch .LBB0_1482
